# baseline (speedup 1.0000x reference)
.Lk2_nodred:
	s_or_b64 exec, exec, s[2:3]
	v_lshrrev_b32_e32 v6, 3, v0
	v_and_b32_e32 v7, 7, v0
	v_lshrrev_b32_e32 v8, 8, v0
	v_bfe_u32 v9, v0, 3, 5
	v_lshlrev_b32_e32 v10, 2, v9
	v_lshl_or_b32 v10, v8, 7, v10
	v_add_u32_e32 v10, 73728, v10
	v_mul_u32_u24_e32 v11, 4608, v8
	v_mul_u32_u24_e32 v12, 576, v7
	v_lshlrev_b32_e32 v13, 4, v9
	v_add3_u32 v11, v11, v12, v13
	s_lshl_b32 s4, s18, 6
	v_or_b32_e32 v14, s4, v6
	v_mov_b32_e32 v15, 0
	v_lshlrev_b64 v[16:17], 8, v[14:15]
	v_lshl_add_u64 v[16:17], s[12:13], 0, v[16:17]
	s_lshl_b32 s2, s16, 7
	s_mov_b32 s3, 0
	v_lshl_add_u64 v[16:17], v[16:17], 0, s[2:3]
	v_lshlrev_b32_e32 v14, 4, v7
	v_lshl_add_u64 v[16:17], v[16:17], 0, v[14:15]
	s_waitcnt lgkmcnt(0)
	s_barrier
	ds_read_b32 v50, v10
	ds_read_b32 v51, v10 offset:256
	ds_read_b32 v52, v10 offset:512
	ds_read_b32 v53, v10 offset:768
	ds_read_b32 v54, v10 offset:1024
	ds_read_b32 v55, v10 offset:1280
	ds_read_b32 v56, v10 offset:1536
	ds_read_b32 v57, v10 offset:1792
	ds_read_b128 v[18:21], v11
	ds_read_b128 v[22:25], v11 offset:9216
	ds_read_b128 v[26:29], v11 offset:18432
	ds_read_b128 v[30:33], v11 offset:27648
	ds_read_b128 v[34:37], v11 offset:36864
	ds_read_b128 v[38:41], v11 offset:46080
	ds_read_b128 v[42:45], v11 offset:55296
	s_waitcnt lgkmcnt(13)
	ds_read_b128 v[46:49], v11 offset:64512
	v_add_f32_e32 v2, v50, v51
	s_waitcnt lgkmcnt(13)
	v_add_f32_e32 v2, v2, v52
	s_waitcnt lgkmcnt(12)
	v_add_f32_e32 v2, v2, v53
	s_waitcnt lgkmcnt(11)
	v_add_f32_e32 v2, v2, v54
	s_waitcnt lgkmcnt(10)
	v_add_f32_e32 v2, v2, v55
	s_waitcnt lgkmcnt(9)
	v_add_f32_e32 v2, v2, v56
	s_waitcnt lgkmcnt(8)
	v_add_f32_e32 v2, v2, v57
	v_div_scale_f32 v3, s[2:3], v2, v2, 1.0
	v_rcp_f32_e32 v4, v3
	v_div_scale_f32 v5, vcc, 1.0, v2, 1.0
	v_fma_f32 v6, -v3, v4, 1.0
	v_fmac_f32_e32 v4, v6, v4
	v_mul_f32_e32 v6, v5, v4
	v_fma_f32 v7, -v3, v6, v5
	v_fmac_f32_e32 v6, v7, v4
	v_fma_f32 v3, -v3, v6, v5
	v_div_fmas_f32 v3, v3, v4, v6
	v_div_fixup_f32 v8, v3, v2, 1.0
	s_waitcnt lgkmcnt(6)
	v_pk_add_f32 v[60:61], v[20:21], v[24:25]
	v_pk_add_f32 v[58:59], v[18:19], v[22:23]
	s_waitcnt lgkmcnt(5)
	v_pk_add_f32 v[60:61], v[60:61], v[28:29]
	v_pk_add_f32 v[58:59], v[58:59], v[26:27]
	s_waitcnt lgkmcnt(4)
	v_pk_add_f32 v[60:61], v[60:61], v[32:33]
	v_pk_add_f32 v[58:59], v[58:59], v[30:31]
	s_waitcnt lgkmcnt(3)
	v_pk_add_f32 v[60:61], v[60:61], v[36:37]
	v_pk_add_f32 v[58:59], v[58:59], v[34:35]
	s_waitcnt lgkmcnt(2)
	v_pk_add_f32 v[60:61], v[60:61], v[40:41]
	v_pk_add_f32 v[58:59], v[58:59], v[38:39]
	s_waitcnt lgkmcnt(1)
	v_pk_add_f32 v[60:61], v[60:61], v[44:45]
	v_pk_add_f32 v[58:59], v[58:59], v[42:43]
	s_waitcnt lgkmcnt(0)
	v_pk_add_f32 v[60:61], v[60:61], v[48:49]
	v_pk_add_f32 v[58:59], v[58:59], v[46:47]
	v_pk_mul_f32 v[60:61], v[60:61], v[8:9] op_sel_hi:[1,0]
	v_pk_mul_f32 v[58:59], v[58:59], v[8:9] op_sel_hi:[1,0]
	global_store_dwordx4 v[16:17], v[58:61], off sc0 sc1
	s_endpgm
